# P0: nt hint also on the transposes' read-once f32 weight loads
# speedup vs baseline: 1.0460x; 1.0038x over previous
.LBB0_11:
	s_or_b64 exec, exec, s[12:13]
	s_lshl_b32 s12, s0, 6
	v_or_b32_e32 v5, s12, v6
	v_mad_i64_i32 v[20:21], s[14:15], v5, s24, 0
	v_cmp_lt_i32_e32 vcc, -1, v2
	v_lshl_add_u64 v[20:21], v[20:21], 2, s[10:11]
	s_lshl_b32 s0, s24, 3
	v_cndmask_b32_e32 v2, 0, v2, vcc
	v_lshl_add_u64 v[20:21], v[2:3], 2, v[20:21]
	v_lshl_add_u64 v[22:23], v[20:21], 0, s[0:1]
	s_lshl_b32 s0, s24, 4
	v_lshl_add_u64 v[24:25], v[20:21], 0, s[0:1]
	s_mul_i32 s0, s24, 24
	v_lshl_add_u64 v[26:27], v[20:21], 0, s[0:1]
	s_lshl_b32 s0, s24, 5
	v_lshl_add_u64 v[28:29], v[20:21], 0, s[0:1]
	s_mul_i32 s0, s24, 40
	v_lshl_add_u64 v[30:31], v[20:21], 0, s[0:1]
	s_mul_i32 s0, s24, 48
	v_lshl_add_u64 v[32:33], v[20:21], 0, s[0:1]
	s_mul_i32 s0, s24, 56
	v_lshl_add_u64 v[34:35], v[20:21], 0, s[0:1]
	s_lshl_b32 s0, s24, 6
	global_load_dword v2, v[20:21], off nt
	global_load_dword v5, v[22:23], off nt
	global_load_dword v38, v[24:25], off nt
	global_load_dword v39, v[26:27], off nt
	global_load_dword v40, v[28:29], off nt
	global_load_dword v41, v[30:31], off nt
	global_load_dword v42, v[32:33], off nt
	global_load_dword v43, v[34:35], off nt
	v_lshl_add_u64 v[22:23], v[20:21], 0, s[0:1]
	s_mul_i32 s0, s24, 0x48
	v_lshl_add_u64 v[24:25], v[20:21], 0, s[0:1]
	s_mul_i32 s0, s24, 0x50
	v_lshl_add_u64 v[26:27], v[20:21], 0, s[0:1]
	s_mul_i32 s0, s24, 0x58
	v_lshl_add_u64 v[28:29], v[20:21], 0, s[0:1]
	s_mul_i32 s0, s24, 0x60
	v_lshl_add_u64 v[30:31], v[20:21], 0, s[0:1]
	s_mul_i32 s0, s24, 0x68
	v_lshl_add_u64 v[32:33], v[20:21], 0, s[0:1]
	s_mul_i32 s0, s24, 0x70
	v_lshl_add_u64 v[34:35], v[20:21], 0, s[0:1]
	s_mul_i32 s0, s24, 0x78
	v_lshl_add_u64 v[36:37], v[20:21], 0, s[0:1]
	s_lshl_b32 s0, s24, 7
	global_load_dword v44, v[22:23], off nt
	global_load_dword v45, v[24:25], off nt
	global_load_dword v46, v[26:27], off nt
	global_load_dword v47, v[28:29], off nt
	global_load_dword v48, v[30:31], off nt
	global_load_dword v49, v[32:33], off nt
	global_load_dword v50, v[34:35], off nt
	global_load_dword v51, v[36:37], off nt
	v_lshl_add_u64 v[22:23], v[20:21], 0, s[0:1]
	s_mul_i32 s0, s24, 0x88
	v_lshl_add_u64 v[24:25], v[20:21], 0, s[0:1]
	s_mul_i32 s0, s24, 0x90
	v_lshl_add_u64 v[26:27], v[20:21], 0, s[0:1]
	s_mul_i32 s0, s24, 0x98
	v_lshl_add_u64 v[28:29], v[20:21], 0, s[0:1]
	s_mul_i32 s0, s24, 0xa0
	v_lshl_add_u64 v[30:31], v[20:21], 0, s[0:1]
	s_mul_i32 s0, s24, 0xa8
	v_lshl_add_u64 v[32:33], v[20:21], 0, s[0:1]
	s_mul_i32 s0, s24, 0xb0
	v_lshl_add_u64 v[34:35], v[20:21], 0, s[0:1]
	s_mul_i32 s0, s24, 0xb8
	v_lshl_add_u64 v[36:37], v[20:21], 0, s[0:1]
	s_mul_i32 s0, s24, 0xc0
	global_load_dword v52, v[22:23], off nt
	global_load_dword v53, v[24:25], off nt
	global_load_dword v54, v[26:27], off nt
	global_load_dword v55, v[28:29], off nt
	global_load_dword v56, v[30:31], off nt
	global_load_dword v57, v[32:33], off nt
	s_nop 0
	global_load_dword v34, v[34:35], off nt
	s_nop 0
	global_load_dword v35, v[36:37], off nt
	v_lshl_add_u64 v[22:23], v[20:21], 0, s[0:1]
	s_mul_i32 s0, s24, 0xc8
	v_lshl_add_u64 v[24:25], v[20:21], 0, s[0:1]
	s_mul_i32 s0, s24, 0xd0
	v_lshl_add_u64 v[26:27], v[20:21], 0, s[0:1]
	s_mul_i32 s0, s24, 0xd8
	v_lshl_add_u64 v[28:29], v[20:21], 0, s[0:1]
	s_mul_i32 s0, s24, 0xe0
	v_lshl_add_u64 v[30:31], v[20:21], 0, s[0:1]
	s_mul_i32 s0, s24, 0xe8
	v_lshl_add_u64 v[32:33], v[20:21], 0, s[0:1]
	s_mul_i32 s0, s24, 0xf0
	global_load_dword v36, v[22:23], off nt
	s_nop 0
	global_load_dword v24, v[24:25], off nt
	s_nop 0
	global_load_dword v25, v[26:27], off nt
	s_nop 0
	global_load_dword v26, v[28:29], off nt
	global_load_dword v27, v[30:31], off nt
	s_nop 0
	global_load_dword v28, v[32:33], off nt
	v_lshl_add_u64 v[22:23], v[20:21], 0, s[0:1]
	s_mul_i32 s0, s24, 0xf8
	v_lshl_add_u64 v[20:21], v[20:21], 0, s[0:1]
	global_load_dword v22, v[22:23], off nt
	s_nop 0
	global_load_dword v20, v[20:21], off nt
	s_ashr_i32 s13, s12, 31
	s_lshl_b64 s[10:11], s[12:13], 1
	s_add_u32 s4, s4, s10
	s_addc_u32 s5, s5, s11
	s_waitcnt vmcnt(31)
	v_cndmask_b32_e32 v2, 0, v2, vcc
	s_waitcnt vmcnt(30)
	v_cndmask_b32_e32 v5, 0, v5, vcc
	ds_write2_b32 v12, v2, v5 offset1:66
	s_waitcnt vmcnt(29)
	v_cndmask_b32_e32 v2, 0, v38, vcc
	s_waitcnt vmcnt(28)
	v_cndmask_b32_e32 v5, 0, v39, vcc
	ds_write2_b32 v12, v2, v5 offset0:132 offset1:198
	s_waitcnt vmcnt(27)
	v_cndmask_b32_e32 v2, 0, v40, vcc
	s_waitcnt vmcnt(26)
	v_cndmask_b32_e32 v5, 0, v41, vcc
	ds_write2_b32 v13, v2, v5 offset0:8 offset1:74
	s_waitcnt vmcnt(25)
	v_cndmask_b32_e32 v2, 0, v42, vcc
	s_waitcnt vmcnt(24)
	v_cndmask_b32_e32 v5, 0, v43, vcc
	ds_write2_b32 v13, v2, v5 offset0:140 offset1:206
	v_or_b32_e32 v42, s23, v7
	v_ashrrev_i32_e32 v43, 31, v42
	v_lshlrev_b64 v[42:43], 11, v[42:43]
	s_waitcnt vmcnt(23)
	v_cndmask_b32_e32 v2, 0, v44, vcc
	s_waitcnt vmcnt(22)
	v_cndmask_b32_e32 v5, 0, v45, vcc
	ds_write2_b32 v14, v2, v5 offset0:16 offset1:82
	s_waitcnt vmcnt(21)
	v_cndmask_b32_e32 v2, 0, v46, vcc
	s_waitcnt vmcnt(20)
	v_cndmask_b32_e32 v5, 0, v47, vcc
	ds_write2_b32 v14, v2, v5 offset0:148 offset1:214
	s_waitcnt vmcnt(19)
	v_cndmask_b32_e32 v2, 0, v48, vcc
	s_waitcnt vmcnt(18)
	v_cndmask_b32_e32 v5, 0, v49, vcc
	ds_write2_b32 v15, v2, v5 offset0:24 offset1:90
	s_waitcnt vmcnt(17)
	v_cndmask_b32_e32 v2, 0, v50, vcc
	s_waitcnt vmcnt(16)
	v_cndmask_b32_e32 v5, 0, v51, vcc
	ds_write2_b32 v15, v2, v5 offset0:156 offset1:222
	s_waitcnt vmcnt(15)
	v_cndmask_b32_e32 v2, 0, v52, vcc
	s_waitcnt vmcnt(14)
	v_cndmask_b32_e32 v5, 0, v53, vcc
	ds_write2_b32 v16, v2, v5 offset0:32 offset1:98
	s_waitcnt vmcnt(13)
	v_cndmask_b32_e32 v2, 0, v54, vcc
	s_waitcnt vmcnt(12)
	v_cndmask_b32_e32 v5, 0, v55, vcc
	ds_write2_b32 v16, v2, v5 offset0:164 offset1:230
	s_waitcnt vmcnt(11)
	v_cndmask_b32_e32 v2, 0, v56, vcc
	s_waitcnt vmcnt(10)
	v_cndmask_b32_e32 v5, 0, v57, vcc
	ds_write2_b32 v17, v2, v5 offset0:40 offset1:106
	s_waitcnt vmcnt(9)
	v_cndmask_b32_e32 v2, 0, v34, vcc
	s_waitcnt vmcnt(8)
	v_cndmask_b32_e32 v5, 0, v35, vcc
	ds_write2_b32 v17, v2, v5 offset0:172 offset1:238
	s_waitcnt vmcnt(7)
	v_cndmask_b32_e32 v2, 0, v36, vcc
	s_waitcnt vmcnt(6)
	v_cndmask_b32_e32 v5, 0, v24, vcc
	ds_write2_b32 v18, v2, v5 offset0:48 offset1:114
	s_waitcnt vmcnt(5)
	v_cndmask_b32_e32 v2, 0, v25, vcc
	s_waitcnt vmcnt(4)
	v_cndmask_b32_e32 v5, 0, v26, vcc
	ds_write2_b32 v18, v2, v5 offset0:180 offset1:246
	s_waitcnt vmcnt(3)
	v_cndmask_b32_e32 v2, 0, v27, vcc
	s_waitcnt vmcnt(2)
	v_cndmask_b32_e32 v5, 0, v28, vcc
	ds_write2_b32 v19, v2, v5 offset0:56 offset1:122
	s_waitcnt vmcnt(1)
	v_cndmask_b32_e32 v2, 0, v22, vcc
	s_waitcnt vmcnt(0)
	v_cndmask_b32_e32 v5, 0, v20, vcc
	ds_write2_b32 v19, v2, v5 offset0:188 offset1:254
	s_waitcnt lgkmcnt(0)
	ds_read2_b32 v[24:25], v8 offset0:33 offset1:41
	ds_read2_b32 v[26:27], v8 offset1:8
	ds_read2_b32 v[28:29], v8 offset0:66 offset1:74
	ds_read2_b32 v[30:31], v8 offset0:99 offset1:107
	ds_read2_b32 v[32:33], v8 offset0:132 offset1:140
	ds_read2_b32 v[34:35], v8 offset0:165 offset1:173
	ds_read2_b32 v[36:37], v8 offset0:198 offset1:206
	ds_read2_b32 v[38:39], v8 offset0:231 offset1:239
	v_mov_b32_e32 v5, v3
	v_lshl_add_u64 v[40:41], s[4:5], 0, v[4:5]
	s_waitcnt lgkmcnt(6)
	v_cvt_pk_bf16_f32 v20, v26, v24
	s_waitcnt lgkmcnt(4)
	v_cvt_pk_bf16_f32 v21, v28, v30
	s_waitcnt lgkmcnt(2)
	v_cvt_pk_bf16_f32 v22, v32, v34
	s_waitcnt lgkmcnt(0)
	v_cvt_pk_bf16_f32 v23, v36, v38
	v_lshl_add_u64 v[42:43], v[40:41], 0, v[42:43]
	v_or_b32_e32 v24, s23, v9
	global_store_dwordx4 v[42:43], v[20:23], off
	s_nop 1
	v_cvt_pk_bf16_f32 v20, v27, v25
	v_ashrrev_i32_e32 v25, 31, v24
	v_cvt_pk_bf16_f32 v21, v29, v31
	v_cvt_pk_bf16_f32 v22, v33, v35
	v_cvt_pk_bf16_f32 v23, v37, v39
	v_lshlrev_b64 v[24:25], 11, v[24:25]
	ds_read2_b32 v[26:27], v8 offset0:49 offset1:57
	ds_read2_b32 v[28:29], v8 offset0:16 offset1:24
	ds_read2_b32 v[30:31], v8 offset0:82 offset1:90
	ds_read2_b32 v[32:33], v8 offset0:115 offset1:123
	ds_read2_b32 v[34:35], v8 offset0:148 offset1:156
	ds_read2_b32 v[36:37], v8 offset0:181 offset1:189
	ds_read2_b32 v[38:39], v8 offset0:214 offset1:222
	ds_read2_b32 v[42:43], v8 offset0:247 offset1:255
	v_lshl_add_u64 v[24:25], v[40:41], 0, v[24:25]
	global_store_dwordx4 v[24:25], v[20:23], off
	v_or_b32_e32 v24, s23, v10
	v_ashrrev_i32_e32 v25, 31, v24
	v_lshlrev_b64 v[24:25], 11, v[24:25]
	s_waitcnt lgkmcnt(6)
	v_cvt_pk_bf16_f32 v20, v28, v26
	s_waitcnt lgkmcnt(4)
	v_cvt_pk_bf16_f32 v21, v30, v32
	s_waitcnt lgkmcnt(2)
	v_cvt_pk_bf16_f32 v22, v34, v36
	s_waitcnt lgkmcnt(0)
	v_cvt_pk_bf16_f32 v23, v38, v42
	v_lshl_add_u64 v[24:25], v[40:41], 0, v[24:25]
	global_store_dwordx4 v[24:25], v[20:23], off
	v_or_b32_e32 v24, s23, v11
	v_ashrrev_i32_e32 v25, 31, v24
	v_lshlrev_b64 v[24:25], 11, v[24:25]
	v_cvt_pk_bf16_f32 v20, v29, v27
	v_cvt_pk_bf16_f32 v21, v31, v33
	v_cvt_pk_bf16_f32 v22, v35, v37
	v_cvt_pk_bf16_f32 v23, v39, v43
	v_lshl_add_u64 v[24:25], v[40:41], 0, v[24:25]
	global_store_dwordx4 v[24:25], v[20:23], off
	s_waitcnt lgkmcnt(0)
